# k_gcn epilogue: drop redundant canonicalising v_max before ReLU (MFMA outputs are never sNaN)
# speedup vs baseline: 1.0006x; 1.0006x over previous
.LBB2_19:
	s_load_dwordx2 s[0:1], s[0:1], 0x28
	v_mov_b32_e32 v35, 0
	v_lshlrev_b32_e32 v34, 4, v83
	s_lshl_b32 s20, s28, 5
	s_mov_b32 s21, 0
	s_waitcnt lgkmcnt(0)
	v_lshl_add_u64 v[36:37], s[0:1], 0, v[34:35]
	v_lshl_add_u64 v[36:37], s[20:21], 2, v[36:37]
	global_load_dwordx4 v[70:73], v[36:37], off
	global_load_dwordx4 v[74:77], v[36:37], off offset:64
	v_mov_b32_e32 v36, v63
	v_mov_b32_e32 v37, v60
	s_waitcnt vmcnt(2)
	v_pk_mul_f32 v[36:37], v[52:53], v[36:37] op_sel_hi:[0,1]
	v_mov_b32_e32 v38, v61
	v_mov_b32_e32 v39, v58
	v_fma_mixlo_f16 v34, v52, v62, 0
	v_cvt_pk_f16_f32 v37, v36, v37
	v_pk_mul_f32 v[38:39], v[52:53], v[38:39] op_sel_hi:[0,1]
	v_pack_b32_f16 v36, v34, v37
	v_cvt_pk_f16_f32 v34, v38, v39
	v_mov_b32_e32 v38, v59
	v_mov_b32_e32 v39, v56
	v_pk_mul_f32 v[38:39], v[52:53], v[38:39] op_sel_hi:[0,1]
	v_cvt_pk_f16_f32 v39, v38, v39
	s_movk_i32 s20, 0x110
	v_alignbit_b32 v38, v39, v34, 16
	v_lshrrev_b32_e32 v39, 16, v39
	v_mad_u64_u32 v[40:41], s[0:1], v51, s20, v[54:55]
	v_alignbit_b32 v37, v34, v37, 16
	v_fma_mixhi_f16 v39, v52, v57, 0
	v_lshlrev_b32_e32 v86, 2, v83
	v_cmp_gt_u32_e32 vcc, 16, v0
	v_mov_b32_e32 v87, 0
	v_mov_b32_e32 v88, 0
	v_mov_b32_e32 v89, 0
	ds_write_b128 v40, v[36:39] offset:5376
	s_and_saveexec_b64 s[0:1], vcc
	s_cbranch_execz .LBB2_21
	v_or_b32_e32 v36, s29, v0
	v_ashrrev_i32_e32 v37, 31, v36
	s_movk_i32 s21, 0x108
	v_mov_b64_e32 v[38:39], s[12:13]
	v_mad_i64_i32 v[38:39], s[12:13], v36, s21, v[38:39]
	v_lshl_add_u64 v[36:37], v[36:37], 2, s[14:15]
	global_load_dwordx2 v[38:39], v[38:39], off
	s_nop 0
	global_load_dword v34, v[36:37], off
	s_waitcnt vmcnt(1)
	s_waitcnt vmcnt(0)
	v_max_f32_e32 v36, 0, v38
	v_max_f32_e32 v37, 0, v39
	v_max_f32_e32 v34, 0, v34
	v_cvt_f16_f32_e32 v88, v36
	v_cvt_f16_f32_e32 v87, v34
	v_cvt_f16_f32_e32 v89, v37
.LBB2_21:
	s_or_b64 exec, exec, s[0:1]
	s_mul_i32 s0, s28, 0x140
	v_or_b32_e32 v34, s0, v1
	s_add_i32 s1, s0, 64
	v_lshl_add_u64 v[36:37], v[34:35], 4, s[16:17]
	v_or_b32_e32 v34, s1, v1
	s_add_i32 s1, s0, 0x80
	v_lshl_add_u64 v[38:39], v[34:35], 4, s[16:17]
	v_or_b32_e32 v34, s1, v1
	s_add_i32 s1, s0, 0xc0
	global_load_dwordx4 v[54:57], v[36:37], off
	global_load_dwordx4 v[58:61], v[38:39], off
	v_lshl_add_u64 v[36:37], v[34:35], 4, s[16:17]
	v_or_b32_e32 v34, s1, v1
	s_addk_i32 s0, 0x100
	v_lshl_add_u64 v[38:39], v[34:35], 4, s[16:17]
	v_or_b32_e32 v34, s0, v1
	v_lshl_add_u64 v[34:35], v[34:35], 4, s[16:17]
	global_load_dwordx4 v[66:69], v[36:37], off
	global_load_dwordx4 v[62:65], v[38:39], off
	global_load_dwordx4 v[46:49], v[34:35], off
	v_lshl_or_b32 v34, s28, 7, v1
	v_ashrrev_i32_e32 v35, 31, v34
	v_lshl_add_u64 v[34:35], v[34:35], 4, s[4:5]
	s_lshl_b32 s4, s28, 4
	s_lshl_b32 s5, s28, 6
	s_add_u32 s0, s18, s5
	s_addc_u32 s1, s19, 0
	s_add_u32 s6, s6, s5
	global_load_dwordx4 v[38:41], v[34:35], off
	global_load_dwordx4 v[42:45], v[34:35], off offset:1024
	v_lshlrev_b32_e32 v34, 2, v86
	s_addc_u32 s7, s7, 0
	global_load_dwordx4 v[78:81], v34, s[0:1]
	global_load_dwordx4 v[50:53], v34, s[6:7]
	s_add_u32 s0, s8, s5
	s_addc_u32 s1, s9, 0
	global_load_dwordx4 v[34:37], v34, s[0:1]
	v_and_b32_e32 v90, 48, v0
	v_mad_u32_u24 v91, v82, s20, v90
	s_waitcnt lgkmcnt(0)
	s_barrier
	ds_read_b128 v[92:95], v91 offset:5376
	s_waitcnt vmcnt(11) lgkmcnt(0)
	v_mfma_f32_16x16x32_f16 v[26:29], v[26:29], v[92:95], v[70:73]
	s_nop 2
	ds_read_b128 v[70:73], v91 offset:5440
	s_andn2_b32 s30, s30, 63
	s_waitcnt vmcnt(10)
	v_mfma_f32_16x16x32_f16 v[30:33], v[30:33], v[92:95], v[74:77]
	s_nop 2
	ds_read_b128 v[74:77], v91 offset:5568
	s_waitcnt lgkmcnt(1)
	v_mfma_f32_16x16x32_f16 v[10:13], v[10:13], v[70:73], v[26:29]
	s_nop 2
	ds_read_b128 v[26:29], v91 offset:5504
	s_waitcnt lgkmcnt(0)
	v_mfma_f32_16x16x32_f16 v[8:11], v[6:9], v[26:29], v[10:13]
	v_mul_u32_u24_e32 v6, 0x150, v82
	v_mfma_f32_16x16x32_f16 v[2:5], v[2:5], v[74:77], v[8:11]
	s_nop 7
	v_max_f32_e32 v7, 0, v2
	v_max_f32_e32 v8, 0, v3
	v_max_f32_e32 v9, 0, v4
	v_max_f32_e32 v10, v5, v5
	v_mfma_f32_16x16x32_f16 v[2:5], v[22:25], v[70:73], v[30:33]
	v_max_f32_e32 v10, 0, v10
	v_cvt_pk_f16_f32 v9, v9, v10
	v_cvt_pk_f16_f32 v8, v7, v8
	v_mfma_f32_16x16x32_f16 v[2:5], v[18:21], v[26:29], v[2:5]
	v_lshlrev_b32_e32 v7, 3, v83
	v_add3_u32 v7, v6, s30, v7
	v_mfma_f32_16x16x32_f16 v[2:5], v[14:17], v[74:77], v[2:5]
	s_nop 7
	v_max_f32_e32 v10, 0, v3
	v_max_f32_e32 v3, v4, v4
	v_max_f32_e32 v2, 0, v2
	v_max_f32_e32 v3, 0, v3
	v_max_f32_e32 v4, 0, v5
	v_cvt_pk_f16_f32 v3, v3, v4
	v_cvt_pk_f16_f32 v2, v2, v10
	ds_write2_b64 v7, v[8:9], v[2:3] offset1:4
	s_and_saveexec_b64 s[0:1], vcc
	s_cbranch_execz .LBB2_23
	s_mov_b32 s5, 0x5040100
	s_mov_b32 s12, 0
	v_mov_b32_e32 v4, 0
	v_perm_b32 v2, v88, v87, s5
	v_and_b32_e32 v3, 0xffff, v89
	v_mov_b32_e32 v5, v4
	v_mul_u32_u24_e32 v7, 0x150, v0
	s_mov_b32 s13, s12
	ds_write_b128 v7, v[2:5] offset:256
	s_mov_b32 s14, s12
	s_mov_b32 s15, s12
	v_mov_b64_e32 v[2:3], s[12:13]
	v_mov_b64_e32 v[4:5], s[14:15]
	ds_write_b128 v7, v[2:5] offset:272
	ds_write_b128 v7, v[2:5] offset:288
	ds_write_b128 v7, v[2:5] offset:304
.LBB2_23:
	s_or_b64 exec, exec, s[0:1]
	v_add_u32_e32 v14, v6, v90
	s_waitcnt lgkmcnt(0)
	s_barrier
	ds_read_b128 v[2:5], v14
	ds_read_b128 v[6:9], v14 offset:64
	s_waitcnt vmcnt(2) lgkmcnt(1)
	v_mfma_f32_16x16x32_f16 v[2:5], v[54:57], v[2:5], v[78:81]
	s_movk_i32 s0, 0x90
	v_or_b32_e32 v15, s4, v86
	s_waitcnt lgkmcnt(0)
	v_mfma_f32_16x16x32_f16 v[2:5], v[58:61], v[6:9], v[2:5]
	ds_read_b128 v[6:9], v14 offset:128
	ds_read_b128 v[10:13], v14 offset:192
	s_waitcnt lgkmcnt(1)
	v_mfma_f32_16x16x32_f16 v[2:5], v[66:69], v[6:9], v[2:5]
	ds_read_b128 v[6:9], v14 offset:256
	s_waitcnt lgkmcnt(1)
	v_mfma_f32_16x16x32_f16 v[2:5], v[62:65], v[10:13], v[2:5]
	v_mov_b32_e32 v10, 0x2600
	v_mad_u32_u24 v10, v82, s0, v10
	v_lshl_add_u32 v11, v15, 1, v10
	s_waitcnt lgkmcnt(0)
	v_mfma_f32_16x16x32_f16 v[2:5], v[46:49], v[6:9], v[2:5]
	v_cmp_gt_u32_e64 s[0:1], 16, v1
	s_nop 6
	v_max_f32_e32 v2, 0, v2
	v_max_f32_e32 v6, 0, v3
	v_max_f32_e32 v3, 0, v4
	v_max_f32_e32 v4, 0, v5
	v_cvt_pk_f16_f32 v3, v3, v4
	v_cvt_pk_f16_f32 v2, v2, v6
	v_add_u32_e32 v6, v10, v90
	ds_write_b64 v11, v[2:3]
	s_waitcnt lgkmcnt(0)
	s_barrier
	ds_read_b128 v[2:5], v6
	ds_read_b128 v[6:9], v6 offset:64
	s_waitcnt vmcnt(1) lgkmcnt(1)
	v_mfma_f32_16x16x32_f16 v[2:5], v[38:41], v[2:5], v[50:53]
	s_waitcnt lgkmcnt(0)
	v_mfma_f32_16x16x32_f16 v[2:5], v[42:45], v[6:9], v[2:5]
	s_nop 7
	v_max_f32_e32 v2, 0, v2
	v_max_f32_e32 v3, 0, v3
	s_waitcnt vmcnt(0)
	v_fma_f32 v2, v2, v34, 0
	v_max_f32_e32 v4, 0, v4
	v_fmac_f32_e32 v2, v3, v35
	v_fmac_f32_e32 v2, v4, v36
	v_max_f32_e32 v3, 0, v5
	v_fmac_f32_e32 v2, v3, v37
	ds_bpermute_b32 v3, v85, v2
	s_waitcnt lgkmcnt(0)
	v_add_f32_e32 v2, v2, v3
	ds_bpermute_b32 v3, v84, v2
	s_and_saveexec_b64 s[4:5], s[0:1]
	s_cbranch_execz .LBB2_25
	v_lshlrev_b32_e32 v1, 2, v82
	v_lshl_or_b32 v1, s28, 6, v1
	s_waitcnt lgkmcnt(0)
	v_add_f32_e32 v2, v2, v3
	ds_write_b32 v1, v2 offset:12032
